# diff attention tile loop: V fragment reads hoisted under the softmax VALU into registers freed by the K fragments; exp/row-sum/bf16 pack in place without register shuffles; v_max3-only integer max cha
# speedup vs baseline: 1.0091x; 1.0091x over previous
.LBB0_1016:
	s_waitcnt lgkmcnt(6)
	v_mfma_f32_32x32x16_bf16 v[82:97], v[166:169], v[118:121], v[82:97]
	s_cmpk_eq_i32 s20, 0xfe00
	s_cselect_b64 s[14:15], -1, 0
	s_cmpk_lg_i32 s20, 0xfe00
	s_cselect_b64 s[16:17], -1, 0
	s_and_b64 vcc, exec, s[14:15]
	s_mov_b64 s[8:9], s[14:15]
	s_waitcnt lgkmcnt(4)
	v_mfma_f32_32x32x16_bf16 v[98:113], v[158:161], v[118:121], v[98:113]
	s_waitcnt lgkmcnt(3)
	v_mfma_f32_32x32x16_bf16 v[82:97], v[154:157], v[122:125], v[82:97]
	s_waitcnt lgkmcnt(1)
	v_mfma_f32_32x32x16_bf16 v[98:113], v[162:165], v[122:125], v[98:113]
	v_mfma_f32_32x32x16_bf16 v[82:97], v[146:149], v[126:129], v[82:97]
	s_waitcnt lgkmcnt(0)
	v_mfma_f32_32x32x16_bf16 v[98:113], v[150:153], v[126:129], v[98:113]
	v_add3_u32 v149, s22, v240, v241
	ds_read_b64_tr_b16 v[150:151], v149 offset:17408
	ds_read_b64_tr_b16 v[152:153], v149 offset:19968
	ds_read_b64_tr_b16 v[154:155], v149 offset:22528
	ds_read_b64_tr_b16 v[156:157], v149 offset:25088
	ds_read_b64_tr_b16 v[158:159], v149 offset:27648
	ds_read_b64_tr_b16 v[160:161], v149 offset:30208
	ds_read_b64_tr_b16 v[162:163], v149 offset:32768
	ds_read_b64_tr_b16 v[164:165], v149 offset:35328
	ds_read_b64_tr_b16 v[166:167], v149 offset:17472
	ds_read_b64_tr_b16 v[168:169], v149 offset:20032
	ds_read_b64_tr_b16 v[170:171], v149 offset:22592
	ds_read_b64_tr_b16 v[172:173], v149 offset:25152
	ds_read_b64_tr_b16 v[174:175], v149 offset:27712
	ds_read_b64_tr_b16 v[176:177], v149 offset:30272
	ds_read_b64_tr_b16 v[216:217], v149 offset:32832
	ds_read_b64_tr_b16 v[218:219], v149 offset:35392
	s_cbranch_vccnz .LBB0_1018
	v_max3_i32 v146, v82, v83, v84
	v_max3_i32 v147, v98, v99, v100
	v_max3_i32 v146, v146, v85, v86
	v_max3_i32 v147, v147, v101, v102
	v_max3_i32 v146, v146, v87, v88
	v_max3_i32 v147, v147, v103, v104
	v_max3_i32 v146, v146, v89, v90
	v_max3_i32 v147, v147, v105, v106
	v_max3_i32 v146, v146, v91, v92
	v_max3_i32 v147, v147, v107, v108
	v_max3_i32 v146, v146, v93, v94
	v_max3_i32 v147, v147, v109, v110
	v_max3_i32 v146, v146, v95, v96
	v_max3_i32 v147, v147, v111, v112
	v_max3_i32 v146, v146, v97, v97
	v_max3_i32 v147, v147, v113, v113
	v_max_i32_e32 v146, v146, v147
	v_cmp_lt_i32_e32 vcc, s54, v146
	s_cmp_lg_u64 vcc, 0
	s_cselect_b64 s[8:9], -1, 0
.LBB0_1018:
	s_andn2_b64 vcc, exec, s[8:9]
	s_cbranch_vccnz .LBB0_1022
	v_max_f32_e32 v146, v99, v99
	v_max_f32_e32 v147, v83, v83
	v_max_f32_e32 v146, v147, v146
	v_max_f32_e32 v147, v100, v100
	v_max_f32_e32 v148, v84, v84
	v_max_f32_e32 v147, v148, v147
	v_max_f32_e32 v148, v101, v101
	v_max_f32_e32 v149, v85, v85
	v_max3_f32 v146, v82, v98, v146
	v_max_f32_e32 v148, v149, v148
	v_max3_f32 v146, v146, v147, v148
	v_max_f32_e32 v147, v102, v102
	v_max_f32_e32 v148, v86, v86
	v_max_f32_e32 v147, v148, v147
	v_max_f32_e32 v148, v103, v103
	v_max_f32_e32 v149, v87, v87
	v_max_f32_e32 v148, v149, v148
	v_max3_f32 v146, v146, v147, v148
	v_max_f32_e32 v147, v104, v104
	v_max_f32_e32 v148, v88, v88
	v_max_f32_e32 v147, v148, v147
	v_max_f32_e32 v148, v105, v105
	v_max_f32_e32 v149, v89, v89
	v_max_f32_e32 v148, v149, v148
	v_max3_f32 v146, v146, v147, v148
	v_max_f32_e32 v147, v106, v106
	v_max_f32_e32 v148, v90, v90
	v_max_f32_e32 v147, v148, v147
	v_max_f32_e32 v148, v107, v107
	v_max_f32_e32 v149, v91, v91
	v_max_f32_e32 v148, v149, v148
	v_max3_f32 v146, v146, v147, v148
	v_max_f32_e32 v147, v108, v108
	v_max_f32_e32 v148, v92, v92
	v_max_f32_e32 v147, v148, v147
	v_max_f32_e32 v148, v109, v109
	v_max_f32_e32 v149, v93, v93
	v_max_f32_e32 v148, v149, v148
	v_max3_f32 v146, v146, v147, v148
	v_max_f32_e32 v147, v110, v110
	v_max_f32_e32 v148, v94, v94
	v_max_f32_e32 v147, v148, v147
	v_max_f32_e32 v148, v111, v111
	v_max_f32_e32 v149, v95, v95
	v_max_f32_e32 v148, v149, v148
	v_max3_f32 v146, v146, v147, v148
	v_max_f32_e32 v147, v112, v112
	v_max_f32_e32 v148, v96, v96
	v_max_f32_e32 v147, v148, v147
	v_max_f32_e32 v148, v113, v113
	v_max_f32_e32 v149, v97, v97
	v_max_f32_e32 v148, v149, v148
	v_max3_f32 v146, v146, v147, v148
	ds_bpermute_b32 v147, v183, v146
	s_andn2_b64 vcc, exec, s[16:17]
	s_waitcnt lgkmcnt(0)
	v_max_f32_e32 v147, v147, v147
	v_max_f32_e32 v146, v146, v147
	v_max_f32_e32 v147, 0, v146
	s_cbranch_vccnz .LBB0_1021
	v_exp_f32_e64 v148, -v147
	s_nop 0
	v_pk_mul_f32 v[64:65], v[64:65], v[148:149] op_sel_hi:[1,0]
	v_pk_mul_f32 v[62:63], v[62:63], v[148:149] op_sel_hi:[1,0]
	v_pk_mul_f32 v[60:61], v[60:61], v[148:149] op_sel_hi:[1,0]
	v_pk_mul_f32 v[58:59], v[58:59], v[148:149] op_sel_hi:[1,0]
	v_pk_mul_f32 v[56:57], v[56:57], v[148:149] op_sel_hi:[1,0]
	v_pk_mul_f32 v[54:55], v[54:55], v[148:149] op_sel_hi:[1,0]
	v_pk_mul_f32 v[52:53], v[52:53], v[148:149] op_sel_hi:[1,0]
	v_pk_mul_f32 v[50:51], v[50:51], v[148:149] op_sel_hi:[1,0]
	v_pk_mul_f32 v[48:49], v[48:49], v[148:149] op_sel_hi:[1,0]
	v_pk_mul_f32 v[46:47], v[46:47], v[148:149] op_sel_hi:[1,0]
	v_pk_mul_f32 v[44:45], v[44:45], v[148:149] op_sel_hi:[1,0]
	v_pk_mul_f32 v[42:43], v[42:43], v[148:149] op_sel_hi:[1,0]
	v_pk_mul_f32 v[40:41], v[40:41], v[148:149] op_sel_hi:[1,0]
	v_pk_mul_f32 v[38:39], v[38:39], v[148:149] op_sel_hi:[1,0]
	v_pk_mul_f32 v[36:37], v[36:37], v[148:149] op_sel_hi:[1,0]
	v_pk_mul_f32 v[34:35], v[34:35], v[148:149] op_sel_hi:[1,0]
	v_pk_mul_f32 v[32:33], v[32:33], v[148:149] op_sel_hi:[1,0]
	v_pk_mul_f32 v[30:31], v[30:31], v[148:149] op_sel_hi:[1,0]
	v_pk_mul_f32 v[28:29], v[28:29], v[148:149] op_sel_hi:[1,0]
	v_pk_mul_f32 v[26:27], v[26:27], v[148:149] op_sel_hi:[1,0]
	v_pk_mul_f32 v[24:25], v[24:25], v[148:149] op_sel_hi:[1,0]
	v_pk_mul_f32 v[22:23], v[22:23], v[148:149] op_sel_hi:[1,0]
	v_pk_mul_f32 v[20:21], v[20:21], v[148:149] op_sel_hi:[1,0]
	v_pk_mul_f32 v[18:19], v[18:19], v[148:149] op_sel_hi:[1,0]
	v_pk_mul_f32 v[16:17], v[16:17], v[148:149] op_sel_hi:[1,0]
	v_pk_mul_f32 v[14:15], v[14:15], v[148:149] op_sel_hi:[1,0]
	v_pk_mul_f32 v[12:13], v[12:13], v[148:149] op_sel_hi:[1,0]
	v_pk_mul_f32 v[10:11], v[10:11], v[148:149] op_sel_hi:[1,0]
	v_pk_mul_f32 v[8:9], v[8:9], v[148:149] op_sel_hi:[1,0]
	v_pk_mul_f32 v[6:7], v[6:7], v[148:149] op_sel_hi:[1,0]
	v_pk_mul_f32 v[4:5], v[4:5], v[148:149] op_sel_hi:[1,0]
	v_pk_mul_f32 v[2:3], v[2:3], v[148:149] op_sel_hi:[1,0]
	v_mul_f32_e32 v205, v205, v148

.LBB0_1022:
	v_exp_f32_e32 v82, v82
	v_exp_f32_e32 v83, v83
	v_exp_f32_e32 v84, v84
	v_exp_f32_e32 v85, v85
	v_exp_f32_e32 v86, v86
	v_exp_f32_e32 v87, v87
	v_exp_f32_e32 v88, v88
	v_exp_f32_e32 v89, v89
	v_exp_f32_e32 v90, v90
	v_exp_f32_e32 v91, v91
	v_exp_f32_e32 v92, v92
	v_exp_f32_e32 v93, v93
	v_exp_f32_e32 v94, v94
	v_exp_f32_e32 v95, v95
	v_exp_f32_e32 v96, v96
	v_exp_f32_e32 v97, v97
	v_exp_f32_e32 v98, v98
	v_exp_f32_e32 v99, v99
	v_exp_f32_e32 v100, v100
	v_exp_f32_e32 v101, v101
	v_exp_f32_e32 v102, v102
	v_exp_f32_e32 v103, v103
	v_exp_f32_e32 v104, v104
	v_exp_f32_e32 v105, v105
	v_exp_f32_e32 v106, v106
	v_exp_f32_e32 v107, v107
	v_exp_f32_e32 v108, v108
	v_exp_f32_e32 v109, v109
	v_exp_f32_e32 v110, v110
	v_exp_f32_e32 v111, v111
	v_exp_f32_e32 v112, v112
	v_exp_f32_e32 v113, v113
	v_pk_add_f32 v[146:147], v[82:83], v[98:99]
	v_pk_add_f32 v[148:149], v[84:85], v[100:101]
	v_pk_add_f32 v[146:147], v[146:147], v[86:87]
	v_pk_add_f32 v[148:149], v[148:149], v[102:103]
	v_pk_add_f32 v[146:147], v[146:147], v[88:89]
	v_pk_add_f32 v[148:149], v[148:149], v[104:105]
	v_pk_add_f32 v[146:147], v[146:147], v[90:91]
	v_pk_add_f32 v[148:149], v[148:149], v[106:107]
	v_pk_add_f32 v[146:147], v[146:147], v[92:93]
	v_pk_add_f32 v[148:149], v[148:149], v[108:109]
	v_pk_add_f32 v[146:147], v[146:147], v[94:95]
	v_pk_add_f32 v[148:149], v[148:149], v[110:111]
	v_pk_add_f32 v[146:147], v[146:147], v[96:97]
	v_pk_add_f32 v[148:149], v[148:149], v[112:113]
	v_pk_add_f32 v[146:147], v[146:147], v[148:149]
	v_cvt_pk_bf16_f32 v82, v82, v83
	v_cvt_pk_bf16_f32 v83, v84, v85
	v_cvt_pk_bf16_f32 v84, v86, v87
	v_cvt_pk_bf16_f32 v85, v88, v89
	v_cvt_pk_bf16_f32 v90, v90, v91
	v_cvt_pk_bf16_f32 v91, v92, v93
	v_cvt_pk_bf16_f32 v92, v94, v95
	v_cvt_pk_bf16_f32 v93, v96, v97
	v_add_f32_e32 v146, v146, v147
	v_cvt_pk_bf16_f32 v86, v98, v99
	v_cvt_pk_bf16_f32 v87, v100, v101
	v_cvt_pk_bf16_f32 v88, v102, v103
	v_cvt_pk_bf16_f32 v89, v104, v105
	v_cvt_pk_bf16_f32 v94, v106, v107
	v_cvt_pk_bf16_f32 v95, v108, v109
	v_cvt_pk_bf16_f32 v96, v110, v111
	v_cvt_pk_bf16_f32 v97, v112, v113
	v_add3_u32 v148, s22, v240, v241
	v_add_f32_e32 v205, v205, v146
	ds_read_b64_tr_b16 v[98:99], v148 offset:17536
	ds_read_b64_tr_b16 v[100:101], v148 offset:20096
	ds_read_b64_tr_b16 v[102:103], v148 offset:22656
	ds_read_b64_tr_b16 v[104:105], v148 offset:25216
	ds_read_b64_tr_b16 v[106:107], v148 offset:27776
	ds_read_b64_tr_b16 v[108:109], v148 offset:30336
	ds_read_b64_tr_b16 v[110:111], v148 offset:32896
	ds_read_b64_tr_b16 v[112:113], v148 offset:35456
	s_waitcnt lgkmcnt(8)
	v_mfma_f32_32x32x16_bf16 v[50:65], v[150:153], v[82:85], v[50:65]
	v_mfma_f32_32x32x16_bf16 v[50:65], v[154:157], v[90:93], v[50:65]
	v_mfma_f32_32x32x16_bf16 v[50:65], v[158:161], v[86:89], v[50:65]
	v_mfma_f32_32x32x16_bf16 v[50:65], v[162:165], v[94:97], v[50:65]
	ds_read_b64_tr_b16 v[150:151], v148 offset:17600
	ds_read_b64_tr_b16 v[152:153], v148 offset:20160
	ds_read_b64_tr_b16 v[154:155], v148 offset:22720
	ds_read_b64_tr_b16 v[156:157], v148 offset:25280
	ds_read_b64_tr_b16 v[158:159], v148 offset:27840
	ds_read_b64_tr_b16 v[160:161], v148 offset:30400
	ds_read_b64_tr_b16 v[162:163], v148 offset:32960
	ds_read_b64_tr_b16 v[164:165], v148 offset:35520
	v_mfma_f32_32x32x16_bf16 v[34:49], v[166:169], v[82:85], v[34:49]
	v_mfma_f32_32x32x16_bf16 v[34:49], v[170:173], v[90:93], v[34:49]
	v_mfma_f32_32x32x16_bf16 v[34:49], v[174:177], v[86:89], v[34:49]
	v_mfma_f32_32x32x16_bf16 v[34:49], v[216:219], v[94:97], v[34:49]
	s_waitcnt lgkmcnt(8)
	v_mfma_f32_32x32x16_bf16 v[18:33], v[98:101], v[82:85], v[18:33]
	v_mfma_f32_32x32x16_bf16 v[18:33], v[102:105], v[90:93], v[18:33]
	v_mfma_f32_32x32x16_bf16 v[18:33], v[106:109], v[86:89], v[18:33]
	v_mfma_f32_32x32x16_bf16 v[18:33], v[110:113], v[94:97], v[18:33]
	s_waitcnt lgkmcnt(0)
	v_mfma_f32_32x32x16_bf16 v[2:17], v[150:153], v[82:85], v[2:17]
	v_mfma_f32_32x32x16_bf16 v[2:17], v[154:157], v[90:93], v[2:17]
	v_mfma_f32_32x32x16_bf16 v[2:17], v[158:161], v[86:89], v[2:17]
	v_mfma_f32_32x32x16_bf16 v[2:17], v[162:165], v[94:97], v[2:17]
	s_andn2_b64 vcc, exec, s[6:7]
	s_cbranch_vccnz .LBB0_1007
